# prep1
# speedup vs baseline: 1.0258x; 1.0258x over previous
.LBB0_3:
	s_cmpk_gt_u32 s10, 0x17f
	s_cbranch_scc0 .LBB0_7
	s_load_dwordx2 s[4:5], s[0:1], 0x0
	s_load_dwordx2 s[6:7], s[0:1], 0x18
	s_load_dwordx2 s[12:13], s[0:1], 0x20
	s_load_dwordx2 s[14:15], s[0:1], 0x38
	s_sub_i32 s8, s10, 0x180
	s_lshl_b32 s9, s8, 4
	s_lshl_b32 s11, s8, 14
	v_and_b32_e32 v1, 63, v0
	v_lshrrev_b32_e32 v2, 6, v0
	v_lshlrev_b32_e32 v1, 6, v1
	v_add_u32_e32 v4, s11, v1
	v_add_u32_e32 v5, 0x1000, v4
	v_add_u32_e32 v6, 0x2000, v4
	v_add_u32_e32 v7, 0x3000, v4
	v_lshl_add_u32 v3, v2, 15, v1
	v_lshlrev_b32_e32 v10, 15, v2
	s_waitcnt lgkmcnt(0)
	s_load_dwordx4 s[16:19], s[12:13], s9
	v_add_u32_e32 v10, s9, v10
	global_load_dwordx4 v[12:15], v4, s[6:7]
	global_load_dwordx4 v[16:19], v4, s[6:7] offset:16
	global_load_dwordx4 v[20:23], v4, s[6:7] offset:32
	global_load_dwordx4 v[24:27], v4, s[6:7] offset:48
	global_load_dwordx4 v[28:31], v5, s[6:7]
	global_load_dwordx4 v[32:35], v5, s[6:7] offset:16
	global_load_dwordx4 v[36:39], v5, s[6:7] offset:32
	global_load_dwordx4 v[40:43], v5, s[6:7] offset:48
	global_load_dwordx4 v[44:47], v6, s[6:7]
	global_load_dwordx4 v[48:51], v6, s[6:7] offset:16
	global_load_dwordx4 v[52:55], v6, s[6:7] offset:32
	global_load_dwordx4 v[56:59], v6, s[6:7] offset:48
	global_load_dwordx4 v[60:63], v7, s[6:7]
	global_load_dwordx4 v[64:67], v7, s[6:7] offset:16
	global_load_dwordx4 v[68:71], v7, s[6:7] offset:32
	global_load_dwordx4 v[72:75], v7, s[6:7] offset:48
	global_load_dwordx4 v[76:79], v3, s[4:5]
	global_load_dwordx4 v[80:83], v3, s[4:5] offset:16
	global_load_dwordx4 v[84:87], v3, s[4:5] offset:32
	global_load_dwordx4 v[88:91], v3, s[4:5] offset:48
	v_add_u32_e32 v9, 0x1000, v3
	global_load_dwordx4 v[92:95], v9, s[4:5]
	global_load_dwordx4 v[96:99], v9, s[4:5] offset:16
	global_load_dwordx4 v[100:103], v9, s[4:5] offset:32
	global_load_dwordx4 v[104:107], v9, s[4:5] offset:48
	v_add_u32_e32 v8, 0x2000, v3
	global_load_dwordx4 v[108:111], v8, s[4:5]
	global_load_dwordx4 v[112:115], v8, s[4:5] offset:16
	global_load_dwordx4 v[116:119], v8, s[4:5] offset:32
	global_load_dwordx4 v[120:123], v8, s[4:5] offset:48
	v_add_u32_e32 v9, 0x3000, v3
	global_load_dwordx4 v[124:127], v9, s[4:5]
	global_load_dwordx4 v[128:131], v9, s[4:5] offset:16
	global_load_dwordx4 v[132:135], v9, s[4:5] offset:32
	global_load_dwordx4 v[136:139], v9, s[4:5] offset:48
	v_add_u32_e32 v8, 0x4000, v3
	global_load_dwordx4 v[140:143], v8, s[4:5]
	global_load_dwordx4 v[144:147], v8, s[4:5] offset:16
	global_load_dwordx4 v[148:151], v8, s[4:5] offset:32
	global_load_dwordx4 v[152:155], v8, s[4:5] offset:48
	v_add_u32_e32 v9, 0x5000, v3
	global_load_dwordx4 v[156:159], v9, s[4:5]
	global_load_dwordx4 v[160:163], v9, s[4:5] offset:16
	global_load_dwordx4 v[164:167], v9, s[4:5] offset:32
	global_load_dwordx4 v[168:171], v9, s[4:5] offset:48
	v_add_u32_e32 v8, 0x6000, v3
	global_load_dwordx4 v[172:175], v8, s[4:5]
	global_load_dwordx4 v[176:179], v8, s[4:5] offset:16
	global_load_dwordx4 v[180:183], v8, s[4:5] offset:32
	global_load_dwordx4 v[184:187], v8, s[4:5] offset:48
	v_add_u32_e32 v9, 0x7000, v3
	global_load_dwordx4 v[188:191], v9, s[4:5]
	global_load_dwordx4 v[192:195], v9, s[4:5] offset:16
	global_load_dwordx4 v[196:199], v9, s[4:5] offset:32
	global_load_dwordx4 v[200:203], v9, s[4:5] offset:48
	s_waitcnt vmcnt(28)
	v_mul_f32_e32 v204, v12, v76
	v_mul_f32_e32 v205, v28, v76
	v_mul_f32_e32 v206, v44, v76
	v_mul_f32_e32 v207, v60, v76
	v_fmac_f32_e32 v204, v13, v77
	v_fmac_f32_e32 v205, v29, v77
	v_fmac_f32_e32 v206, v45, v77
	v_fmac_f32_e32 v207, v61, v77
	v_fmac_f32_e32 v204, v14, v78
	v_fmac_f32_e32 v205, v30, v78
	v_fmac_f32_e32 v206, v46, v78
	v_fmac_f32_e32 v207, v62, v78
	v_fmac_f32_e32 v204, v15, v79
	v_fmac_f32_e32 v205, v31, v79
	v_fmac_f32_e32 v206, v47, v79
	v_fmac_f32_e32 v207, v63, v79
	v_fmac_f32_e32 v204, v16, v80
	v_fmac_f32_e32 v205, v32, v80
	v_fmac_f32_e32 v206, v48, v80
	v_fmac_f32_e32 v207, v64, v80
	v_fmac_f32_e32 v204, v17, v81
	v_fmac_f32_e32 v205, v33, v81
	v_fmac_f32_e32 v206, v49, v81
	v_fmac_f32_e32 v207, v65, v81
	v_fmac_f32_e32 v204, v18, v82
	v_fmac_f32_e32 v205, v34, v82
	v_fmac_f32_e32 v206, v50, v82
	v_fmac_f32_e32 v207, v66, v82
	v_fmac_f32_e32 v204, v19, v83
	v_fmac_f32_e32 v205, v35, v83
	v_fmac_f32_e32 v206, v51, v83
	v_fmac_f32_e32 v207, v67, v83
	v_fmac_f32_e32 v204, v20, v84
	v_fmac_f32_e32 v205, v36, v84
	v_fmac_f32_e32 v206, v52, v84
	v_fmac_f32_e32 v207, v68, v84
	v_fmac_f32_e32 v204, v21, v85
	v_fmac_f32_e32 v205, v37, v85
	v_fmac_f32_e32 v206, v53, v85
	v_fmac_f32_e32 v207, v69, v85
	v_fmac_f32_e32 v204, v22, v86
	v_fmac_f32_e32 v205, v38, v86
	v_fmac_f32_e32 v206, v54, v86
	v_fmac_f32_e32 v207, v70, v86
	v_fmac_f32_e32 v204, v23, v87
	v_fmac_f32_e32 v205, v39, v87
	v_fmac_f32_e32 v206, v55, v87
	v_fmac_f32_e32 v207, v71, v87
	v_fmac_f32_e32 v204, v24, v88
	v_fmac_f32_e32 v205, v40, v88
	v_fmac_f32_e32 v206, v56, v88
	v_fmac_f32_e32 v207, v72, v88
	v_fmac_f32_e32 v204, v25, v89
	v_fmac_f32_e32 v205, v41, v89
	v_fmac_f32_e32 v206, v57, v89
	v_fmac_f32_e32 v207, v73, v89
	v_fmac_f32_e32 v204, v26, v90
	v_fmac_f32_e32 v205, v42, v90
	v_fmac_f32_e32 v206, v58, v90
	v_fmac_f32_e32 v207, v74, v90
	v_fmac_f32_e32 v204, v27, v91
	v_fmac_f32_e32 v205, v43, v91
	v_fmac_f32_e32 v206, v59, v91
	v_fmac_f32_e32 v207, v75, v91
	s_waitcnt vmcnt(24)
	v_mul_f32_e32 v208, v12, v92
	v_mul_f32_e32 v209, v28, v92
	v_mul_f32_e32 v210, v44, v92
	v_mul_f32_e32 v211, v60, v92
	v_fmac_f32_e32 v208, v13, v93
	v_fmac_f32_e32 v209, v29, v93
	v_fmac_f32_e32 v210, v45, v93
	v_fmac_f32_e32 v211, v61, v93
	v_fmac_f32_e32 v208, v14, v94
	v_fmac_f32_e32 v209, v30, v94
	v_fmac_f32_e32 v210, v46, v94
	v_fmac_f32_e32 v211, v62, v94
	v_fmac_f32_e32 v208, v15, v95
	v_fmac_f32_e32 v209, v31, v95
	v_fmac_f32_e32 v210, v47, v95
	v_fmac_f32_e32 v211, v63, v95
	v_fmac_f32_e32 v208, v16, v96
	v_fmac_f32_e32 v209, v32, v96
	v_fmac_f32_e32 v210, v48, v96
	v_fmac_f32_e32 v211, v64, v96
	v_fmac_f32_e32 v208, v17, v97
	v_fmac_f32_e32 v209, v33, v97
	v_fmac_f32_e32 v210, v49, v97
	v_fmac_f32_e32 v211, v65, v97
	v_fmac_f32_e32 v208, v18, v98
	v_fmac_f32_e32 v209, v34, v98
	v_fmac_f32_e32 v210, v50, v98
	v_fmac_f32_e32 v211, v66, v98
	v_fmac_f32_e32 v208, v19, v99
	v_fmac_f32_e32 v209, v35, v99
	v_fmac_f32_e32 v210, v51, v99
	v_fmac_f32_e32 v211, v67, v99
	v_fmac_f32_e32 v208, v20, v100
	v_fmac_f32_e32 v209, v36, v100
	v_fmac_f32_e32 v210, v52, v100
	v_fmac_f32_e32 v211, v68, v100
	v_fmac_f32_e32 v208, v21, v101
	v_fmac_f32_e32 v209, v37, v101
	v_fmac_f32_e32 v210, v53, v101
	v_fmac_f32_e32 v211, v69, v101
	v_fmac_f32_e32 v208, v22, v102
	v_fmac_f32_e32 v209, v38, v102
	v_fmac_f32_e32 v210, v54, v102
	v_fmac_f32_e32 v211, v70, v102
	v_fmac_f32_e32 v208, v23, v103
	v_fmac_f32_e32 v209, v39, v103
	v_fmac_f32_e32 v210, v55, v103
	v_fmac_f32_e32 v211, v71, v103
	v_fmac_f32_e32 v208, v24, v104
	v_fmac_f32_e32 v209, v40, v104
	v_fmac_f32_e32 v210, v56, v104
	v_fmac_f32_e32 v211, v72, v104
	v_fmac_f32_e32 v208, v25, v105
	v_fmac_f32_e32 v209, v41, v105
	v_fmac_f32_e32 v210, v57, v105
	v_fmac_f32_e32 v211, v73, v105
	v_fmac_f32_e32 v208, v26, v106
	v_fmac_f32_e32 v209, v42, v106
	v_fmac_f32_e32 v210, v58, v106
	v_fmac_f32_e32 v211, v74, v106
	v_fmac_f32_e32 v208, v27, v107
	v_fmac_f32_e32 v209, v43, v107
	v_fmac_f32_e32 v210, v59, v107
	v_fmac_f32_e32 v211, v75, v107
	s_waitcnt vmcnt(20)
	v_mul_f32_e32 v212, v12, v108
	v_mul_f32_e32 v213, v28, v108
	v_mul_f32_e32 v214, v44, v108
	v_mul_f32_e32 v215, v60, v108
	v_fmac_f32_e32 v212, v13, v109
	v_fmac_f32_e32 v213, v29, v109
	v_fmac_f32_e32 v214, v45, v109
	v_fmac_f32_e32 v215, v61, v109
	v_fmac_f32_e32 v212, v14, v110
	v_fmac_f32_e32 v213, v30, v110
	v_fmac_f32_e32 v214, v46, v110
	v_fmac_f32_e32 v215, v62, v110
	v_fmac_f32_e32 v212, v15, v111
	v_fmac_f32_e32 v213, v31, v111
	v_fmac_f32_e32 v214, v47, v111
	v_fmac_f32_e32 v215, v63, v111
	v_fmac_f32_e32 v212, v16, v112
	v_fmac_f32_e32 v213, v32, v112
	v_fmac_f32_e32 v214, v48, v112
	v_fmac_f32_e32 v215, v64, v112
	v_fmac_f32_e32 v212, v17, v113
	v_fmac_f32_e32 v213, v33, v113
	v_fmac_f32_e32 v214, v49, v113
	v_fmac_f32_e32 v215, v65, v113
	v_fmac_f32_e32 v212, v18, v114
	v_fmac_f32_e32 v213, v34, v114
	v_fmac_f32_e32 v214, v50, v114
	v_fmac_f32_e32 v215, v66, v114
	v_fmac_f32_e32 v212, v19, v115
	v_fmac_f32_e32 v213, v35, v115
	v_fmac_f32_e32 v214, v51, v115
	v_fmac_f32_e32 v215, v67, v115
	v_fmac_f32_e32 v212, v20, v116
	v_fmac_f32_e32 v213, v36, v116
	v_fmac_f32_e32 v214, v52, v116
	v_fmac_f32_e32 v215, v68, v116
	v_fmac_f32_e32 v212, v21, v117
	v_fmac_f32_e32 v213, v37, v117
	v_fmac_f32_e32 v214, v53, v117
	v_fmac_f32_e32 v215, v69, v117
	v_fmac_f32_e32 v212, v22, v118
	v_fmac_f32_e32 v213, v38, v118
	v_fmac_f32_e32 v214, v54, v118
	v_fmac_f32_e32 v215, v70, v118
	v_fmac_f32_e32 v212, v23, v119
	v_fmac_f32_e32 v213, v39, v119
	v_fmac_f32_e32 v214, v55, v119
	v_fmac_f32_e32 v215, v71, v119
	v_fmac_f32_e32 v212, v24, v120
	v_fmac_f32_e32 v213, v40, v120
	v_fmac_f32_e32 v214, v56, v120
	v_fmac_f32_e32 v215, v72, v120
	v_fmac_f32_e32 v212, v25, v121
	v_fmac_f32_e32 v213, v41, v121
	v_fmac_f32_e32 v214, v57, v121
	v_fmac_f32_e32 v215, v73, v121
	v_fmac_f32_e32 v212, v26, v122
	v_fmac_f32_e32 v213, v42, v122
	v_fmac_f32_e32 v214, v58, v122
	v_fmac_f32_e32 v215, v74, v122
	v_fmac_f32_e32 v212, v27, v123
	v_fmac_f32_e32 v213, v43, v123
	v_fmac_f32_e32 v214, v59, v123
	v_fmac_f32_e32 v215, v75, v123
	s_waitcnt vmcnt(16)
	v_mul_f32_e32 v216, v12, v124
	v_mul_f32_e32 v217, v28, v124
	v_mul_f32_e32 v218, v44, v124
	v_mul_f32_e32 v219, v60, v124
	v_fmac_f32_e32 v216, v13, v125
	v_fmac_f32_e32 v217, v29, v125
	v_fmac_f32_e32 v218, v45, v125
	v_fmac_f32_e32 v219, v61, v125
	v_fmac_f32_e32 v216, v14, v126
	v_fmac_f32_e32 v217, v30, v126
	v_fmac_f32_e32 v218, v46, v126
	v_fmac_f32_e32 v219, v62, v126
	v_fmac_f32_e32 v216, v15, v127
	v_fmac_f32_e32 v217, v31, v127
	v_fmac_f32_e32 v218, v47, v127
	v_fmac_f32_e32 v219, v63, v127
	v_fmac_f32_e32 v216, v16, v128
	v_fmac_f32_e32 v217, v32, v128
	v_fmac_f32_e32 v218, v48, v128
	v_fmac_f32_e32 v219, v64, v128
	v_fmac_f32_e32 v216, v17, v129
	v_fmac_f32_e32 v217, v33, v129
	v_fmac_f32_e32 v218, v49, v129
	v_fmac_f32_e32 v219, v65, v129
	v_fmac_f32_e32 v216, v18, v130
	v_fmac_f32_e32 v217, v34, v130
	v_fmac_f32_e32 v218, v50, v130
	v_fmac_f32_e32 v219, v66, v130
	v_fmac_f32_e32 v216, v19, v131
	v_fmac_f32_e32 v217, v35, v131
	v_fmac_f32_e32 v218, v51, v131
	v_fmac_f32_e32 v219, v67, v131
	v_fmac_f32_e32 v216, v20, v132
	v_fmac_f32_e32 v217, v36, v132
	v_fmac_f32_e32 v218, v52, v132
	v_fmac_f32_e32 v219, v68, v132
	v_fmac_f32_e32 v216, v21, v133
	v_fmac_f32_e32 v217, v37, v133
	v_fmac_f32_e32 v218, v53, v133
	v_fmac_f32_e32 v219, v69, v133
	v_fmac_f32_e32 v216, v22, v134
	v_fmac_f32_e32 v217, v38, v134
	v_fmac_f32_e32 v218, v54, v134
	v_fmac_f32_e32 v219, v70, v134
	v_fmac_f32_e32 v216, v23, v135
	v_fmac_f32_e32 v217, v39, v135
	v_fmac_f32_e32 v218, v55, v135
	v_fmac_f32_e32 v219, v71, v135
	v_fmac_f32_e32 v216, v24, v136
	v_fmac_f32_e32 v217, v40, v136
	v_fmac_f32_e32 v218, v56, v136
	v_fmac_f32_e32 v219, v72, v136
	v_fmac_f32_e32 v216, v25, v137
	v_fmac_f32_e32 v217, v41, v137
	v_fmac_f32_e32 v218, v57, v137
	v_fmac_f32_e32 v219, v73, v137
	v_fmac_f32_e32 v216, v26, v138
	v_fmac_f32_e32 v217, v42, v138
	v_fmac_f32_e32 v218, v58, v138
	v_fmac_f32_e32 v219, v74, v138
	v_fmac_f32_e32 v216, v27, v139
	v_fmac_f32_e32 v217, v43, v139
	v_fmac_f32_e32 v218, v59, v139
	v_fmac_f32_e32 v219, v75, v139
	s_waitcnt vmcnt(12)
	v_mul_f32_e32 v220, v12, v140
	v_mul_f32_e32 v221, v28, v140
	v_mul_f32_e32 v222, v44, v140
	v_mul_f32_e32 v223, v60, v140
	v_fmac_f32_e32 v220, v13, v141
	v_fmac_f32_e32 v221, v29, v141
	v_fmac_f32_e32 v222, v45, v141
	v_fmac_f32_e32 v223, v61, v141
	v_fmac_f32_e32 v220, v14, v142
	v_fmac_f32_e32 v221, v30, v142
	v_fmac_f32_e32 v222, v46, v142
	v_fmac_f32_e32 v223, v62, v142
	v_fmac_f32_e32 v220, v15, v143
	v_fmac_f32_e32 v221, v31, v143
	v_fmac_f32_e32 v222, v47, v143
	v_fmac_f32_e32 v223, v63, v143
	v_fmac_f32_e32 v220, v16, v144
	v_fmac_f32_e32 v221, v32, v144
	v_fmac_f32_e32 v222, v48, v144
	v_fmac_f32_e32 v223, v64, v144
	v_fmac_f32_e32 v220, v17, v145
	v_fmac_f32_e32 v221, v33, v145
	v_fmac_f32_e32 v222, v49, v145
	v_fmac_f32_e32 v223, v65, v145
	v_fmac_f32_e32 v220, v18, v146
	v_fmac_f32_e32 v221, v34, v146
	v_fmac_f32_e32 v222, v50, v146
	v_fmac_f32_e32 v223, v66, v146
	v_fmac_f32_e32 v220, v19, v147
	v_fmac_f32_e32 v221, v35, v147
	v_fmac_f32_e32 v222, v51, v147
	v_fmac_f32_e32 v223, v67, v147
	v_fmac_f32_e32 v220, v20, v148
	v_fmac_f32_e32 v221, v36, v148
	v_fmac_f32_e32 v222, v52, v148
	v_fmac_f32_e32 v223, v68, v148
	v_fmac_f32_e32 v220, v21, v149
	v_fmac_f32_e32 v221, v37, v149
	v_fmac_f32_e32 v222, v53, v149
	v_fmac_f32_e32 v223, v69, v149
	v_fmac_f32_e32 v220, v22, v150
	v_fmac_f32_e32 v221, v38, v150
	v_fmac_f32_e32 v222, v54, v150
	v_fmac_f32_e32 v223, v70, v150
	v_fmac_f32_e32 v220, v23, v151
	v_fmac_f32_e32 v221, v39, v151
	v_fmac_f32_e32 v222, v55, v151
	v_fmac_f32_e32 v223, v71, v151
	v_fmac_f32_e32 v220, v24, v152
	v_fmac_f32_e32 v221, v40, v152
	v_fmac_f32_e32 v222, v56, v152
	v_fmac_f32_e32 v223, v72, v152
	v_fmac_f32_e32 v220, v25, v153
	v_fmac_f32_e32 v221, v41, v153
	v_fmac_f32_e32 v222, v57, v153
	v_fmac_f32_e32 v223, v73, v153
	v_fmac_f32_e32 v220, v26, v154
	v_fmac_f32_e32 v221, v42, v154
	v_fmac_f32_e32 v222, v58, v154
	v_fmac_f32_e32 v223, v74, v154
	v_fmac_f32_e32 v220, v27, v155
	v_fmac_f32_e32 v221, v43, v155
	v_fmac_f32_e32 v222, v59, v155
	v_fmac_f32_e32 v223, v75, v155
	s_waitcnt vmcnt(8)
	v_mul_f32_e32 v224, v12, v156
	v_mul_f32_e32 v225, v28, v156
	v_mul_f32_e32 v226, v44, v156
	v_mul_f32_e32 v227, v60, v156
	v_fmac_f32_e32 v224, v13, v157
	v_fmac_f32_e32 v225, v29, v157
	v_fmac_f32_e32 v226, v45, v157
	v_fmac_f32_e32 v227, v61, v157
	v_fmac_f32_e32 v224, v14, v158
	v_fmac_f32_e32 v225, v30, v158
	v_fmac_f32_e32 v226, v46, v158
	v_fmac_f32_e32 v227, v62, v158
	v_fmac_f32_e32 v224, v15, v159
	v_fmac_f32_e32 v225, v31, v159
	v_fmac_f32_e32 v226, v47, v159
	v_fmac_f32_e32 v227, v63, v159
	v_fmac_f32_e32 v224, v16, v160
	v_fmac_f32_e32 v225, v32, v160
	v_fmac_f32_e32 v226, v48, v160
	v_fmac_f32_e32 v227, v64, v160
	v_fmac_f32_e32 v224, v17, v161
	v_fmac_f32_e32 v225, v33, v161
	v_fmac_f32_e32 v226, v49, v161
	v_fmac_f32_e32 v227, v65, v161
	v_fmac_f32_e32 v224, v18, v162
	v_fmac_f32_e32 v225, v34, v162
	v_fmac_f32_e32 v226, v50, v162
	v_fmac_f32_e32 v227, v66, v162
	v_fmac_f32_e32 v224, v19, v163
	v_fmac_f32_e32 v225, v35, v163
	v_fmac_f32_e32 v226, v51, v163
	v_fmac_f32_e32 v227, v67, v163
	v_fmac_f32_e32 v224, v20, v164
	v_fmac_f32_e32 v225, v36, v164
	v_fmac_f32_e32 v226, v52, v164
	v_fmac_f32_e32 v227, v68, v164
	v_fmac_f32_e32 v224, v21, v165
	v_fmac_f32_e32 v225, v37, v165
	v_fmac_f32_e32 v226, v53, v165
	v_fmac_f32_e32 v227, v69, v165
	v_fmac_f32_e32 v224, v22, v166
	v_fmac_f32_e32 v225, v38, v166
	v_fmac_f32_e32 v226, v54, v166
	v_fmac_f32_e32 v227, v70, v166
	v_fmac_f32_e32 v224, v23, v167
	v_fmac_f32_e32 v225, v39, v167
	v_fmac_f32_e32 v226, v55, v167
	v_fmac_f32_e32 v227, v71, v167
	v_fmac_f32_e32 v224, v24, v168
	v_fmac_f32_e32 v225, v40, v168
	v_fmac_f32_e32 v226, v56, v168
	v_fmac_f32_e32 v227, v72, v168
	v_fmac_f32_e32 v224, v25, v169
	v_fmac_f32_e32 v225, v41, v169
	v_fmac_f32_e32 v226, v57, v169
	v_fmac_f32_e32 v227, v73, v169
	v_fmac_f32_e32 v224, v26, v170
	v_fmac_f32_e32 v225, v42, v170
	v_fmac_f32_e32 v226, v58, v170
	v_fmac_f32_e32 v227, v74, v170
	v_fmac_f32_e32 v224, v27, v171
	v_fmac_f32_e32 v225, v43, v171
	v_fmac_f32_e32 v226, v59, v171
	v_fmac_f32_e32 v227, v75, v171
	s_waitcnt vmcnt(4)
	v_mul_f32_e32 v228, v12, v172
	v_mul_f32_e32 v229, v28, v172
	v_mul_f32_e32 v230, v44, v172
	v_mul_f32_e32 v231, v60, v172
	v_fmac_f32_e32 v228, v13, v173
	v_fmac_f32_e32 v229, v29, v173
	v_fmac_f32_e32 v230, v45, v173
	v_fmac_f32_e32 v231, v61, v173
	v_fmac_f32_e32 v228, v14, v174
	v_fmac_f32_e32 v229, v30, v174
	v_fmac_f32_e32 v230, v46, v174
	v_fmac_f32_e32 v231, v62, v174
	v_fmac_f32_e32 v228, v15, v175
	v_fmac_f32_e32 v229, v31, v175
	v_fmac_f32_e32 v230, v47, v175
	v_fmac_f32_e32 v231, v63, v175
	v_fmac_f32_e32 v228, v16, v176
	v_fmac_f32_e32 v229, v32, v176
	v_fmac_f32_e32 v230, v48, v176
	v_fmac_f32_e32 v231, v64, v176
	v_fmac_f32_e32 v228, v17, v177
	v_fmac_f32_e32 v229, v33, v177
	v_fmac_f32_e32 v230, v49, v177
	v_fmac_f32_e32 v231, v65, v177
	v_fmac_f32_e32 v228, v18, v178
	v_fmac_f32_e32 v229, v34, v178
	v_fmac_f32_e32 v230, v50, v178
	v_fmac_f32_e32 v231, v66, v178
	v_fmac_f32_e32 v228, v19, v179
	v_fmac_f32_e32 v229, v35, v179
	v_fmac_f32_e32 v230, v51, v179
	v_fmac_f32_e32 v231, v67, v179
	v_fmac_f32_e32 v228, v20, v180
	v_fmac_f32_e32 v229, v36, v180
	v_fmac_f32_e32 v230, v52, v180
	v_fmac_f32_e32 v231, v68, v180
	v_fmac_f32_e32 v228, v21, v181
	v_fmac_f32_e32 v229, v37, v181
	v_fmac_f32_e32 v230, v53, v181
	v_fmac_f32_e32 v231, v69, v181
	v_fmac_f32_e32 v228, v22, v182
	v_fmac_f32_e32 v229, v38, v182
	v_fmac_f32_e32 v230, v54, v182
	v_fmac_f32_e32 v231, v70, v182
	v_fmac_f32_e32 v228, v23, v183
	v_fmac_f32_e32 v229, v39, v183
	v_fmac_f32_e32 v230, v55, v183
	v_fmac_f32_e32 v231, v71, v183
	v_fmac_f32_e32 v228, v24, v184
	v_fmac_f32_e32 v229, v40, v184
	v_fmac_f32_e32 v230, v56, v184
	v_fmac_f32_e32 v231, v72, v184
	v_fmac_f32_e32 v228, v25, v185
	v_fmac_f32_e32 v229, v41, v185
	v_fmac_f32_e32 v230, v57, v185
	v_fmac_f32_e32 v231, v73, v185
	v_fmac_f32_e32 v228, v26, v186
	v_fmac_f32_e32 v229, v42, v186
	v_fmac_f32_e32 v230, v58, v186
	v_fmac_f32_e32 v231, v74, v186
	v_fmac_f32_e32 v228, v27, v187
	v_fmac_f32_e32 v229, v43, v187
	v_fmac_f32_e32 v230, v59, v187
	v_fmac_f32_e32 v231, v75, v187
	s_waitcnt vmcnt(0)
	v_mul_f32_e32 v232, v12, v188
	v_mul_f32_e32 v233, v28, v188
	v_mul_f32_e32 v234, v44, v188
	v_mul_f32_e32 v235, v60, v188
	v_fmac_f32_e32 v232, v13, v189
	v_fmac_f32_e32 v233, v29, v189
	v_fmac_f32_e32 v234, v45, v189
	v_fmac_f32_e32 v235, v61, v189
	v_fmac_f32_e32 v232, v14, v190
	v_fmac_f32_e32 v233, v30, v190
	v_fmac_f32_e32 v234, v46, v190
	v_fmac_f32_e32 v235, v62, v190
	v_fmac_f32_e32 v232, v15, v191
	v_fmac_f32_e32 v233, v31, v191
	v_fmac_f32_e32 v234, v47, v191
	v_fmac_f32_e32 v235, v63, v191
	v_fmac_f32_e32 v232, v16, v192
	v_fmac_f32_e32 v233, v32, v192
	v_fmac_f32_e32 v234, v48, v192
	v_fmac_f32_e32 v235, v64, v192
	v_fmac_f32_e32 v232, v17, v193
	v_fmac_f32_e32 v233, v33, v193
	v_fmac_f32_e32 v234, v49, v193
	v_fmac_f32_e32 v235, v65, v193
	v_fmac_f32_e32 v232, v18, v194
	v_fmac_f32_e32 v233, v34, v194
	v_fmac_f32_e32 v234, v50, v194
	v_fmac_f32_e32 v235, v66, v194
	v_fmac_f32_e32 v232, v19, v195
	v_fmac_f32_e32 v233, v35, v195
	v_fmac_f32_e32 v234, v51, v195
	v_fmac_f32_e32 v235, v67, v195
	v_fmac_f32_e32 v232, v20, v196
	v_fmac_f32_e32 v233, v36, v196
	v_fmac_f32_e32 v234, v52, v196
	v_fmac_f32_e32 v235, v68, v196
	v_fmac_f32_e32 v232, v21, v197
	v_fmac_f32_e32 v233, v37, v197
	v_fmac_f32_e32 v234, v53, v197
	v_fmac_f32_e32 v235, v69, v197
	v_fmac_f32_e32 v232, v22, v198
	v_fmac_f32_e32 v233, v38, v198
	v_fmac_f32_e32 v234, v54, v198
	v_fmac_f32_e32 v235, v70, v198
	v_fmac_f32_e32 v232, v23, v199
	v_fmac_f32_e32 v233, v39, v199
	v_fmac_f32_e32 v234, v55, v199
	v_fmac_f32_e32 v235, v71, v199
	v_fmac_f32_e32 v232, v24, v200
	v_fmac_f32_e32 v233, v40, v200
	v_fmac_f32_e32 v234, v56, v200
	v_fmac_f32_e32 v235, v72, v200
	v_fmac_f32_e32 v232, v25, v201
	v_fmac_f32_e32 v233, v41, v201
	v_fmac_f32_e32 v234, v57, v201
	v_fmac_f32_e32 v235, v73, v201
	v_fmac_f32_e32 v232, v26, v202
	v_fmac_f32_e32 v233, v42, v202
	v_fmac_f32_e32 v234, v58, v202
	v_fmac_f32_e32 v235, v74, v202
	v_fmac_f32_e32 v232, v27, v203
	v_fmac_f32_e32 v233, v43, v203
	v_fmac_f32_e32 v234, v59, v203
	v_fmac_f32_e32 v235, v75, v203
	s_nop 1
	v_add_f32_dpp v204, v204, v204 quad_perm:[1,0,3,2] row_mask:0xf bank_mask:0xf
	v_add_f32_dpp v205, v205, v205 quad_perm:[1,0,3,2] row_mask:0xf bank_mask:0xf
	v_add_f32_dpp v206, v206, v206 quad_perm:[1,0,3,2] row_mask:0xf bank_mask:0xf
	v_add_f32_dpp v207, v207, v207 quad_perm:[1,0,3,2] row_mask:0xf bank_mask:0xf
	v_add_f32_dpp v208, v208, v208 quad_perm:[1,0,3,2] row_mask:0xf bank_mask:0xf
	v_add_f32_dpp v209, v209, v209 quad_perm:[1,0,3,2] row_mask:0xf bank_mask:0xf
	v_add_f32_dpp v210, v210, v210 quad_perm:[1,0,3,2] row_mask:0xf bank_mask:0xf
	v_add_f32_dpp v211, v211, v211 quad_perm:[1,0,3,2] row_mask:0xf bank_mask:0xf
	v_add_f32_dpp v212, v212, v212 quad_perm:[1,0,3,2] row_mask:0xf bank_mask:0xf
	v_add_f32_dpp v213, v213, v213 quad_perm:[1,0,3,2] row_mask:0xf bank_mask:0xf
	v_add_f32_dpp v214, v214, v214 quad_perm:[1,0,3,2] row_mask:0xf bank_mask:0xf
	v_add_f32_dpp v215, v215, v215 quad_perm:[1,0,3,2] row_mask:0xf bank_mask:0xf
	v_add_f32_dpp v216, v216, v216 quad_perm:[1,0,3,2] row_mask:0xf bank_mask:0xf
	v_add_f32_dpp v217, v217, v217 quad_perm:[1,0,3,2] row_mask:0xf bank_mask:0xf
	v_add_f32_dpp v218, v218, v218 quad_perm:[1,0,3,2] row_mask:0xf bank_mask:0xf
	v_add_f32_dpp v219, v219, v219 quad_perm:[1,0,3,2] row_mask:0xf bank_mask:0xf
	v_add_f32_dpp v220, v220, v220 quad_perm:[1,0,3,2] row_mask:0xf bank_mask:0xf
	v_add_f32_dpp v221, v221, v221 quad_perm:[1,0,3,2] row_mask:0xf bank_mask:0xf
	v_add_f32_dpp v222, v222, v222 quad_perm:[1,0,3,2] row_mask:0xf bank_mask:0xf
	v_add_f32_dpp v223, v223, v223 quad_perm:[1,0,3,2] row_mask:0xf bank_mask:0xf
	v_add_f32_dpp v224, v224, v224 quad_perm:[1,0,3,2] row_mask:0xf bank_mask:0xf
	v_add_f32_dpp v225, v225, v225 quad_perm:[1,0,3,2] row_mask:0xf bank_mask:0xf
	v_add_f32_dpp v226, v226, v226 quad_perm:[1,0,3,2] row_mask:0xf bank_mask:0xf
	v_add_f32_dpp v227, v227, v227 quad_perm:[1,0,3,2] row_mask:0xf bank_mask:0xf
	v_add_f32_dpp v228, v228, v228 quad_perm:[1,0,3,2] row_mask:0xf bank_mask:0xf
	v_add_f32_dpp v229, v229, v229 quad_perm:[1,0,3,2] row_mask:0xf bank_mask:0xf
	v_add_f32_dpp v230, v230, v230 quad_perm:[1,0,3,2] row_mask:0xf bank_mask:0xf
	v_add_f32_dpp v231, v231, v231 quad_perm:[1,0,3,2] row_mask:0xf bank_mask:0xf
	v_add_f32_dpp v232, v232, v232 quad_perm:[1,0,3,2] row_mask:0xf bank_mask:0xf
	v_add_f32_dpp v233, v233, v233 quad_perm:[1,0,3,2] row_mask:0xf bank_mask:0xf
	v_add_f32_dpp v234, v234, v234 quad_perm:[1,0,3,2] row_mask:0xf bank_mask:0xf
	v_add_f32_dpp v235, v235, v235 quad_perm:[1,0,3,2] row_mask:0xf bank_mask:0xf
	v_add_f32_dpp v204, v204, v204 quad_perm:[2,3,0,1] row_mask:0xf bank_mask:0xf
	v_add_f32_dpp v205, v205, v205 quad_perm:[2,3,0,1] row_mask:0xf bank_mask:0xf
	v_add_f32_dpp v206, v206, v206 quad_perm:[2,3,0,1] row_mask:0xf bank_mask:0xf
	v_add_f32_dpp v207, v207, v207 quad_perm:[2,3,0,1] row_mask:0xf bank_mask:0xf
	v_add_f32_dpp v208, v208, v208 quad_perm:[2,3,0,1] row_mask:0xf bank_mask:0xf
	v_add_f32_dpp v209, v209, v209 quad_perm:[2,3,0,1] row_mask:0xf bank_mask:0xf
	v_add_f32_dpp v210, v210, v210 quad_perm:[2,3,0,1] row_mask:0xf bank_mask:0xf
	v_add_f32_dpp v211, v211, v211 quad_perm:[2,3,0,1] row_mask:0xf bank_mask:0xf
	v_add_f32_dpp v212, v212, v212 quad_perm:[2,3,0,1] row_mask:0xf bank_mask:0xf
	v_add_f32_dpp v213, v213, v213 quad_perm:[2,3,0,1] row_mask:0xf bank_mask:0xf
	v_add_f32_dpp v214, v214, v214 quad_perm:[2,3,0,1] row_mask:0xf bank_mask:0xf
	v_add_f32_dpp v215, v215, v215 quad_perm:[2,3,0,1] row_mask:0xf bank_mask:0xf
	v_add_f32_dpp v216, v216, v216 quad_perm:[2,3,0,1] row_mask:0xf bank_mask:0xf
	v_add_f32_dpp v217, v217, v217 quad_perm:[2,3,0,1] row_mask:0xf bank_mask:0xf
	v_add_f32_dpp v218, v218, v218 quad_perm:[2,3,0,1] row_mask:0xf bank_mask:0xf
	v_add_f32_dpp v219, v219, v219 quad_perm:[2,3,0,1] row_mask:0xf bank_mask:0xf
	v_add_f32_dpp v220, v220, v220 quad_perm:[2,3,0,1] row_mask:0xf bank_mask:0xf
	v_add_f32_dpp v221, v221, v221 quad_perm:[2,3,0,1] row_mask:0xf bank_mask:0xf
	v_add_f32_dpp v222, v222, v222 quad_perm:[2,3,0,1] row_mask:0xf bank_mask:0xf
	v_add_f32_dpp v223, v223, v223 quad_perm:[2,3,0,1] row_mask:0xf bank_mask:0xf
	v_add_f32_dpp v224, v224, v224 quad_perm:[2,3,0,1] row_mask:0xf bank_mask:0xf
	v_add_f32_dpp v225, v225, v225 quad_perm:[2,3,0,1] row_mask:0xf bank_mask:0xf
	v_add_f32_dpp v226, v226, v226 quad_perm:[2,3,0,1] row_mask:0xf bank_mask:0xf
	v_add_f32_dpp v227, v227, v227 quad_perm:[2,3,0,1] row_mask:0xf bank_mask:0xf
	v_add_f32_dpp v228, v228, v228 quad_perm:[2,3,0,1] row_mask:0xf bank_mask:0xf
	v_add_f32_dpp v229, v229, v229 quad_perm:[2,3,0,1] row_mask:0xf bank_mask:0xf
	v_add_f32_dpp v230, v230, v230 quad_perm:[2,3,0,1] row_mask:0xf bank_mask:0xf
	v_add_f32_dpp v231, v231, v231 quad_perm:[2,3,0,1] row_mask:0xf bank_mask:0xf
	v_add_f32_dpp v232, v232, v232 quad_perm:[2,3,0,1] row_mask:0xf bank_mask:0xf
	v_add_f32_dpp v233, v233, v233 quad_perm:[2,3,0,1] row_mask:0xf bank_mask:0xf
	v_add_f32_dpp v234, v234, v234 quad_perm:[2,3,0,1] row_mask:0xf bank_mask:0xf
	v_add_f32_dpp v235, v235, v235 quad_perm:[2,3,0,1] row_mask:0xf bank_mask:0xf
	v_add_f32_dpp v204, v204, v204 row_half_mirror row_mask:0xf bank_mask:0xf
	v_add_f32_dpp v205, v205, v205 row_half_mirror row_mask:0xf bank_mask:0xf
	v_add_f32_dpp v206, v206, v206 row_half_mirror row_mask:0xf bank_mask:0xf
	v_add_f32_dpp v207, v207, v207 row_half_mirror row_mask:0xf bank_mask:0xf
	v_add_f32_dpp v208, v208, v208 row_half_mirror row_mask:0xf bank_mask:0xf
	v_add_f32_dpp v209, v209, v209 row_half_mirror row_mask:0xf bank_mask:0xf
	v_add_f32_dpp v210, v210, v210 row_half_mirror row_mask:0xf bank_mask:0xf
	v_add_f32_dpp v211, v211, v211 row_half_mirror row_mask:0xf bank_mask:0xf
	v_add_f32_dpp v212, v212, v212 row_half_mirror row_mask:0xf bank_mask:0xf
	v_add_f32_dpp v213, v213, v213 row_half_mirror row_mask:0xf bank_mask:0xf
	v_add_f32_dpp v214, v214, v214 row_half_mirror row_mask:0xf bank_mask:0xf
	v_add_f32_dpp v215, v215, v215 row_half_mirror row_mask:0xf bank_mask:0xf
	v_add_f32_dpp v216, v216, v216 row_half_mirror row_mask:0xf bank_mask:0xf
	v_add_f32_dpp v217, v217, v217 row_half_mirror row_mask:0xf bank_mask:0xf
	v_add_f32_dpp v218, v218, v218 row_half_mirror row_mask:0xf bank_mask:0xf
	v_add_f32_dpp v219, v219, v219 row_half_mirror row_mask:0xf bank_mask:0xf
	v_add_f32_dpp v220, v220, v220 row_half_mirror row_mask:0xf bank_mask:0xf
	v_add_f32_dpp v221, v221, v221 row_half_mirror row_mask:0xf bank_mask:0xf
	v_add_f32_dpp v222, v222, v222 row_half_mirror row_mask:0xf bank_mask:0xf
	v_add_f32_dpp v223, v223, v223 row_half_mirror row_mask:0xf bank_mask:0xf
	v_add_f32_dpp v224, v224, v224 row_half_mirror row_mask:0xf bank_mask:0xf
	v_add_f32_dpp v225, v225, v225 row_half_mirror row_mask:0xf bank_mask:0xf
	v_add_f32_dpp v226, v226, v226 row_half_mirror row_mask:0xf bank_mask:0xf
	v_add_f32_dpp v227, v227, v227 row_half_mirror row_mask:0xf bank_mask:0xf
	v_add_f32_dpp v228, v228, v228 row_half_mirror row_mask:0xf bank_mask:0xf
	v_add_f32_dpp v229, v229, v229 row_half_mirror row_mask:0xf bank_mask:0xf
	v_add_f32_dpp v230, v230, v230 row_half_mirror row_mask:0xf bank_mask:0xf
	v_add_f32_dpp v231, v231, v231 row_half_mirror row_mask:0xf bank_mask:0xf
	v_add_f32_dpp v232, v232, v232 row_half_mirror row_mask:0xf bank_mask:0xf
	v_add_f32_dpp v233, v233, v233 row_half_mirror row_mask:0xf bank_mask:0xf
	v_add_f32_dpp v234, v234, v234 row_half_mirror row_mask:0xf bank_mask:0xf
	v_add_f32_dpp v235, v235, v235 row_half_mirror row_mask:0xf bank_mask:0xf
	v_add_f32_dpp v204, v204, v204 row_mirror row_mask:0xf bank_mask:0xf
	v_add_f32_dpp v205, v205, v205 row_mirror row_mask:0xf bank_mask:0xf
	v_add_f32_dpp v206, v206, v206 row_mirror row_mask:0xf bank_mask:0xf
	v_add_f32_dpp v207, v207, v207 row_mirror row_mask:0xf bank_mask:0xf
	v_add_f32_dpp v208, v208, v208 row_mirror row_mask:0xf bank_mask:0xf
	v_add_f32_dpp v209, v209, v209 row_mirror row_mask:0xf bank_mask:0xf
	v_add_f32_dpp v210, v210, v210 row_mirror row_mask:0xf bank_mask:0xf
	v_add_f32_dpp v211, v211, v211 row_mirror row_mask:0xf bank_mask:0xf
	v_add_f32_dpp v212, v212, v212 row_mirror row_mask:0xf bank_mask:0xf
	v_add_f32_dpp v213, v213, v213 row_mirror row_mask:0xf bank_mask:0xf
	v_add_f32_dpp v214, v214, v214 row_mirror row_mask:0xf bank_mask:0xf
	v_add_f32_dpp v215, v215, v215 row_mirror row_mask:0xf bank_mask:0xf
	v_add_f32_dpp v216, v216, v216 row_mirror row_mask:0xf bank_mask:0xf
	v_add_f32_dpp v217, v217, v217 row_mirror row_mask:0xf bank_mask:0xf
	v_add_f32_dpp v218, v218, v218 row_mirror row_mask:0xf bank_mask:0xf
	v_add_f32_dpp v219, v219, v219 row_mirror row_mask:0xf bank_mask:0xf
	v_add_f32_dpp v220, v220, v220 row_mirror row_mask:0xf bank_mask:0xf
	v_add_f32_dpp v221, v221, v221 row_mirror row_mask:0xf bank_mask:0xf
	v_add_f32_dpp v222, v222, v222 row_mirror row_mask:0xf bank_mask:0xf
	v_add_f32_dpp v223, v223, v223 row_mirror row_mask:0xf bank_mask:0xf
	v_add_f32_dpp v224, v224, v224 row_mirror row_mask:0xf bank_mask:0xf
	v_add_f32_dpp v225, v225, v225 row_mirror row_mask:0xf bank_mask:0xf
	v_add_f32_dpp v226, v226, v226 row_mirror row_mask:0xf bank_mask:0xf
	v_add_f32_dpp v227, v227, v227 row_mirror row_mask:0xf bank_mask:0xf
	v_add_f32_dpp v228, v228, v228 row_mirror row_mask:0xf bank_mask:0xf
	v_add_f32_dpp v229, v229, v229 row_mirror row_mask:0xf bank_mask:0xf
	v_add_f32_dpp v230, v230, v230 row_mirror row_mask:0xf bank_mask:0xf
	v_add_f32_dpp v231, v231, v231 row_mirror row_mask:0xf bank_mask:0xf
	v_add_f32_dpp v232, v232, v232 row_mirror row_mask:0xf bank_mask:0xf
	v_add_f32_dpp v233, v233, v233 row_mirror row_mask:0xf bank_mask:0xf
	v_add_f32_dpp v234, v234, v234 row_mirror row_mask:0xf bank_mask:0xf
	v_add_f32_dpp v235, v235, v235 row_mirror row_mask:0xf bank_mask:0xf
	v_add_f32_dpp v204, v204, v204 row_bcast:15 row_mask:0xa bank_mask:0xf
	v_add_f32_dpp v205, v205, v205 row_bcast:15 row_mask:0xa bank_mask:0xf
	v_add_f32_dpp v206, v206, v206 row_bcast:15 row_mask:0xa bank_mask:0xf
	v_add_f32_dpp v207, v207, v207 row_bcast:15 row_mask:0xa bank_mask:0xf
	v_add_f32_dpp v208, v208, v208 row_bcast:15 row_mask:0xa bank_mask:0xf
	v_add_f32_dpp v209, v209, v209 row_bcast:15 row_mask:0xa bank_mask:0xf
	v_add_f32_dpp v210, v210, v210 row_bcast:15 row_mask:0xa bank_mask:0xf
	v_add_f32_dpp v211, v211, v211 row_bcast:15 row_mask:0xa bank_mask:0xf
	v_add_f32_dpp v212, v212, v212 row_bcast:15 row_mask:0xa bank_mask:0xf
	v_add_f32_dpp v213, v213, v213 row_bcast:15 row_mask:0xa bank_mask:0xf
	v_add_f32_dpp v214, v214, v214 row_bcast:15 row_mask:0xa bank_mask:0xf
	v_add_f32_dpp v215, v215, v215 row_bcast:15 row_mask:0xa bank_mask:0xf
	v_add_f32_dpp v216, v216, v216 row_bcast:15 row_mask:0xa bank_mask:0xf
	v_add_f32_dpp v217, v217, v217 row_bcast:15 row_mask:0xa bank_mask:0xf
	v_add_f32_dpp v218, v218, v218 row_bcast:15 row_mask:0xa bank_mask:0xf
	v_add_f32_dpp v219, v219, v219 row_bcast:15 row_mask:0xa bank_mask:0xf
	v_add_f32_dpp v220, v220, v220 row_bcast:15 row_mask:0xa bank_mask:0xf
	v_add_f32_dpp v221, v221, v221 row_bcast:15 row_mask:0xa bank_mask:0xf
	v_add_f32_dpp v222, v222, v222 row_bcast:15 row_mask:0xa bank_mask:0xf
	v_add_f32_dpp v223, v223, v223 row_bcast:15 row_mask:0xa bank_mask:0xf
	v_add_f32_dpp v224, v224, v224 row_bcast:15 row_mask:0xa bank_mask:0xf
	v_add_f32_dpp v225, v225, v225 row_bcast:15 row_mask:0xa bank_mask:0xf
	v_add_f32_dpp v226, v226, v226 row_bcast:15 row_mask:0xa bank_mask:0xf
	v_add_f32_dpp v227, v227, v227 row_bcast:15 row_mask:0xa bank_mask:0xf
	v_add_f32_dpp v228, v228, v228 row_bcast:15 row_mask:0xa bank_mask:0xf
	v_add_f32_dpp v229, v229, v229 row_bcast:15 row_mask:0xa bank_mask:0xf
	v_add_f32_dpp v230, v230, v230 row_bcast:15 row_mask:0xa bank_mask:0xf
	v_add_f32_dpp v231, v231, v231 row_bcast:15 row_mask:0xa bank_mask:0xf
	v_add_f32_dpp v232, v232, v232 row_bcast:15 row_mask:0xa bank_mask:0xf
	v_add_f32_dpp v233, v233, v233 row_bcast:15 row_mask:0xa bank_mask:0xf
	v_add_f32_dpp v234, v234, v234 row_bcast:15 row_mask:0xa bank_mask:0xf
	v_add_f32_dpp v235, v235, v235 row_bcast:15 row_mask:0xa bank_mask:0xf
	v_add_f32_dpp v204, v204, v204 row_bcast:31 row_mask:0xc bank_mask:0xf
	v_add_f32_dpp v205, v205, v205 row_bcast:31 row_mask:0xc bank_mask:0xf
	v_add_f32_dpp v206, v206, v206 row_bcast:31 row_mask:0xc bank_mask:0xf
	v_add_f32_dpp v207, v207, v207 row_bcast:31 row_mask:0xc bank_mask:0xf
	v_add_f32_dpp v208, v208, v208 row_bcast:31 row_mask:0xc bank_mask:0xf
	v_add_f32_dpp v209, v209, v209 row_bcast:31 row_mask:0xc bank_mask:0xf
	v_add_f32_dpp v210, v210, v210 row_bcast:31 row_mask:0xc bank_mask:0xf
	v_add_f32_dpp v211, v211, v211 row_bcast:31 row_mask:0xc bank_mask:0xf
	v_add_f32_dpp v212, v212, v212 row_bcast:31 row_mask:0xc bank_mask:0xf
	v_add_f32_dpp v213, v213, v213 row_bcast:31 row_mask:0xc bank_mask:0xf
	v_add_f32_dpp v214, v214, v214 row_bcast:31 row_mask:0xc bank_mask:0xf
	v_add_f32_dpp v215, v215, v215 row_bcast:31 row_mask:0xc bank_mask:0xf
	v_add_f32_dpp v216, v216, v216 row_bcast:31 row_mask:0xc bank_mask:0xf
	v_add_f32_dpp v217, v217, v217 row_bcast:31 row_mask:0xc bank_mask:0xf
	v_add_f32_dpp v218, v218, v218 row_bcast:31 row_mask:0xc bank_mask:0xf
	v_add_f32_dpp v219, v219, v219 row_bcast:31 row_mask:0xc bank_mask:0xf
	v_add_f32_dpp v220, v220, v220 row_bcast:31 row_mask:0xc bank_mask:0xf
	v_add_f32_dpp v221, v221, v221 row_bcast:31 row_mask:0xc bank_mask:0xf
	v_add_f32_dpp v222, v222, v222 row_bcast:31 row_mask:0xc bank_mask:0xf
	v_add_f32_dpp v223, v223, v223 row_bcast:31 row_mask:0xc bank_mask:0xf
	v_add_f32_dpp v224, v224, v224 row_bcast:31 row_mask:0xc bank_mask:0xf
	v_add_f32_dpp v225, v225, v225 row_bcast:31 row_mask:0xc bank_mask:0xf
	v_add_f32_dpp v226, v226, v226 row_bcast:31 row_mask:0xc bank_mask:0xf
	v_add_f32_dpp v227, v227, v227 row_bcast:31 row_mask:0xc bank_mask:0xf
	v_add_f32_dpp v228, v228, v228 row_bcast:31 row_mask:0xc bank_mask:0xf
	v_add_f32_dpp v229, v229, v229 row_bcast:31 row_mask:0xc bank_mask:0xf
	v_add_f32_dpp v230, v230, v230 row_bcast:31 row_mask:0xc bank_mask:0xf
	v_add_f32_dpp v231, v231, v231 row_bcast:31 row_mask:0xc bank_mask:0xf
	v_add_f32_dpp v232, v232, v232 row_bcast:31 row_mask:0xc bank_mask:0xf
	v_add_f32_dpp v233, v233, v233 row_bcast:31 row_mask:0xc bank_mask:0xf
	v_add_f32_dpp v234, v234, v234 row_bcast:31 row_mask:0xc bank_mask:0xf
	v_add_f32_dpp v235, v235, v235 row_bcast:31 row_mask:0xc bank_mask:0xf
	v_cmp_eq_u32_e32 vcc, 0xfc0, v1
	s_and_saveexec_b64 s[20:21], vcc
	s_waitcnt lgkmcnt(0)
	v_add_f32_e32 v204, s16, v204
	v_add_f32_e32 v205, s17, v205
	v_add_f32_e32 v206, s18, v206
	v_add_f32_e32 v207, s19, v207
	v_add_f32_e32 v208, s16, v208
	v_add_f32_e32 v209, s17, v209
	v_add_f32_e32 v210, s18, v210
	v_add_f32_e32 v211, s19, v211
	v_add_f32_e32 v212, s16, v212
	v_add_f32_e32 v213, s17, v213
	v_add_f32_e32 v214, s18, v214
	v_add_f32_e32 v215, s19, v215
	v_add_f32_e32 v216, s16, v216
	v_add_f32_e32 v217, s17, v217
	v_add_f32_e32 v218, s18, v218
	v_add_f32_e32 v219, s19, v219
	v_add_f32_e32 v220, s16, v220
	v_add_f32_e32 v221, s17, v221
	v_add_f32_e32 v222, s18, v222
	v_add_f32_e32 v223, s19, v223
	v_add_f32_e32 v224, s16, v224
	v_add_f32_e32 v225, s17, v225
	v_add_f32_e32 v226, s18, v226
	v_add_f32_e32 v227, s19, v227
	v_add_f32_e32 v228, s16, v228
	v_add_f32_e32 v229, s17, v229
	v_add_f32_e32 v230, s18, v230
	v_add_f32_e32 v231, s19, v231
	v_add_f32_e32 v232, s16, v232
	v_add_f32_e32 v233, s17, v233
	v_add_f32_e32 v234, s18, v234
	v_add_f32_e32 v235, s19, v235
	v_mul_f32_e32 v204, 0x4038aa3b, v204
	v_mul_f32_e32 v205, 0x4038aa3b, v205
	v_mul_f32_e32 v206, 0x4038aa3b, v206
	v_mul_f32_e32 v207, 0x4038aa3b, v207
	v_mul_f32_e32 v208, 0x4038aa3b, v208
	v_mul_f32_e32 v209, 0x4038aa3b, v209
	v_mul_f32_e32 v210, 0x4038aa3b, v210
	v_mul_f32_e32 v211, 0x4038aa3b, v211
	v_mul_f32_e32 v212, 0x4038aa3b, v212
	v_mul_f32_e32 v213, 0x4038aa3b, v213
	v_mul_f32_e32 v214, 0x4038aa3b, v214
	v_mul_f32_e32 v215, 0x4038aa3b, v215
	v_mul_f32_e32 v216, 0x4038aa3b, v216
	v_mul_f32_e32 v217, 0x4038aa3b, v217
	v_mul_f32_e32 v218, 0x4038aa3b, v218
	v_mul_f32_e32 v219, 0x4038aa3b, v219
	v_mul_f32_e32 v220, 0x4038aa3b, v220
	v_mul_f32_e32 v221, 0x4038aa3b, v221
	v_mul_f32_e32 v222, 0x4038aa3b, v222
	v_mul_f32_e32 v223, 0x4038aa3b, v223
	v_mul_f32_e32 v224, 0x4038aa3b, v224
	v_mul_f32_e32 v225, 0x4038aa3b, v225
	v_mul_f32_e32 v226, 0x4038aa3b, v226
	v_mul_f32_e32 v227, 0x4038aa3b, v227
	v_mul_f32_e32 v228, 0x4038aa3b, v228
	v_mul_f32_e32 v229, 0x4038aa3b, v229
	v_mul_f32_e32 v230, 0x4038aa3b, v230
	v_mul_f32_e32 v231, 0x4038aa3b, v231
	v_mul_f32_e32 v232, 0x4038aa3b, v232
	v_mul_f32_e32 v233, 0x4038aa3b, v233
	v_mul_f32_e32 v234, 0x4038aa3b, v234
	v_mul_f32_e32 v235, 0x4038aa3b, v235
	global_store_dwordx4 v10, v[204:207], s[14:15]
	v_add_u32_e32 v9, 0x1000, v10
	global_store_dwordx4 v9, v[208:211], s[14:15]
	v_add_u32_e32 v8, 0x2000, v10
	global_store_dwordx4 v8, v[212:215], s[14:15]
	v_add_u32_e32 v9, 0x3000, v10
	global_store_dwordx4 v9, v[216:219], s[14:15]
	v_add_u32_e32 v8, 0x4000, v10
	global_store_dwordx4 v8, v[220:223], s[14:15]
	v_add_u32_e32 v9, 0x5000, v10
	global_store_dwordx4 v9, v[224:227], s[14:15]
	v_add_u32_e32 v8, 0x6000, v10
	global_store_dwordx4 v8, v[228:231], s[14:15]
	v_add_u32_e32 v9, 0x7000, v10
	global_store_dwordx4 v9, v[232:235], s[14:15]
	s_endpgm

	.amdhsa_kernel _Z11prep_kernelPKfS0_S0_S0_S0_PDF16_S1_Pf
		.amdhsa_group_segment_fixed_size 0
		.amdhsa_private_segment_fixed_size 0
		.amdhsa_kernarg_size 64
		.amdhsa_user_sgpr_count 2
		.amdhsa_user_sgpr_dispatch_ptr 0
		.amdhsa_user_sgpr_queue_ptr 0
		.amdhsa_user_sgpr_kernarg_segment_ptr 1
		.amdhsa_user_sgpr_dispatch_id 0
		.amdhsa_user_sgpr_kernarg_preload_length 0
		.amdhsa_user_sgpr_kernarg_preload_offset 0
		.amdhsa_user_sgpr_private_segment_size 0
		.amdhsa_uses_dynamic_stack 0
		.amdhsa_enable_private_segment 0
		.amdhsa_system_sgpr_workgroup_id_x 1
		.amdhsa_system_sgpr_workgroup_id_y 0
		.amdhsa_system_sgpr_workgroup_id_z 0
		.amdhsa_system_sgpr_workgroup_info 0
		.amdhsa_system_vgpr_workitem_id 0
		.amdhsa_next_free_vgpr 236
		.amdhsa_next_free_sgpr 24
		.amdhsa_accum_offset 236
		.amdhsa_reserve_vcc 1
		.amdhsa_float_round_mode_32 0
		.amdhsa_float_round_mode_16_64 0
		.amdhsa_float_denorm_mode_32 3
		.amdhsa_float_denorm_mode_16_64 3
		.amdhsa_dx10_clamp 1
		.amdhsa_ieee_mode 1
		.amdhsa_fp16_overflow 0
		.amdhsa_tg_split 0
		.amdhsa_exception_fp_ieee_invalid_op 0
		.amdhsa_exception_fp_denorm_src 0
		.amdhsa_exception_fp_ieee_div_zero 0
		.amdhsa_exception_fp_ieee_overflow 0
		.amdhsa_exception_fp_ieee_underflow 0
		.amdhsa_exception_fp_ieee_inexact 0
		.amdhsa_exception_int_div_zero 0
	.end_amdhsa_kernel

amdhsa.kernels:
  - .agpr_count:     0
    .args:
      - .actual_access:  read_only
        .address_space:  global
        .offset:         0
        .size:           8
        .value_kind:     global_buffer
      - .actual_access:  read_only
        .address_space:  global
        .offset:         8
        .size:           8
        .value_kind:     global_buffer
      - .actual_access:  read_only
        .address_space:  global
        .offset:         16
        .size:           8
        .value_kind:     global_buffer
      - .actual_access:  read_only
        .address_space:  global
        .offset:         24
        .size:           8
        .value_kind:     global_buffer
      - .actual_access:  read_only
        .address_space:  global
        .offset:         32
        .size:           8
        .value_kind:     global_buffer
      - .actual_access:  write_only
        .address_space:  global
        .offset:         40
        .size:           8
        .value_kind:     global_buffer
      - .actual_access:  write_only
        .address_space:  global
        .offset:         48
        .size:           8
        .value_kind:     global_buffer
      - .actual_access:  write_only
        .address_space:  global
        .offset:         56
        .size:           8
        .value_kind:     global_buffer
    .group_segment_fixed_size: 0
    .kernarg_segment_align: 8
    .kernarg_segment_size: 64
    .language:       OpenCL C
    .language_version:
      - 2
      - 0
    .max_flat_workgroup_size: 256
    .name:           _Z11prep_kernelPKfS0_S0_S0_S0_PDF16_S1_Pf
    .private_segment_fixed_size: 0
    .sgpr_count:     30
    .sgpr_spill_count: 0
    .symbol:         _Z11prep_kernelPKfS0_S0_S0_S0_PDF16_S1_Pf.kd
    .uniform_work_group_size: 1
    .uses_dynamic_stack: false
    .vgpr_count:     236
    .vgpr_spill_count: 0
    .wavefront_size: 64
  - .agpr_count:     0
    .args:
      - .address_space:  global
        .offset:         0
        .size:           8
        .value_kind:     global_buffer
      - .address_space:  global
        .offset:         8
        .size:           8
        .value_kind:     global_buffer
      - .actual_access:  read_only
        .address_space:  global
        .offset:         16
        .size:           8
        .value_kind:     global_buffer
      - .address_space:  global
        .offset:         24
        .size:           8
        .value_kind:     global_buffer
      - .actual_access:  read_only
        .address_space:  global
        .offset:         32
        .size:           8
        .value_kind:     global_buffer
      - .actual_access:  read_only
        .address_space:  global
        .offset:         40
        .size:           8
        .value_kind:     global_buffer
      - .actual_access:  read_only
        .address_space:  global
        .offset:         48
        .size:           8
        .value_kind:     global_buffer
      - .actual_access:  write_only
        .address_space:  global
        .offset:         56
        .size:           8
        .value_kind:     global_buffer
      - .actual_access:  write_only
        .address_space:  global
        .offset:         64
        .size:           8
        .value_kind:     global_buffer
    .group_segment_fixed_size: 131072
    .kernarg_segment_align: 8
    .kernarg_segment_size: 72
    .language:       OpenCL C
    .language_version:
      - 2
      - 0
    .max_flat_workgroup_size: 512
    .name:           _Z11main_kernelPKDF16_PKfPKiS0_S2_S2_S2_PfS5_
    .private_segment_fixed_size: 0
    .sgpr_count:     108
    .sgpr_spill_count: 0
    .symbol:         _Z11main_kernelPKDF16_PKfPKiS0_S2_S2_S2_PfS5_.kd
    .uniform_work_group_size: 1
    .uses_dynamic_stack: false
    .vgpr_count:     256
    .vgpr_spill_count: 0
    .wavefront_size: 64
  - .agpr_count:     0
    .args:
      - .actual_access:  read_only
        .address_space:  global
        .offset:         0
        .size:           8
        .value_kind:     global_buffer
      - .actual_access:  read_only
        .address_space:  global
        .offset:         8
        .size:           8
        .value_kind:     global_buffer
      - .actual_access:  write_only
        .address_space:  global
        .offset:         16
        .size:           8
        .value_kind:     global_buffer
    .group_segment_fixed_size: 32
    .kernarg_segment_align: 8
    .kernarg_segment_size: 24
    .language:       OpenCL C
    .language_version:
      - 2
      - 0
    .max_flat_workgroup_size: 256
    .name:           _Z14combine_kernelPKfS0_Pf
    .private_segment_fixed_size: 0
    .sgpr_count:     26
    .sgpr_spill_count: 0
    .symbol:         _Z14combine_kernelPKfS0_Pf.kd
    .uniform_work_group_size: 1
    .uses_dynamic_stack: false
    .vgpr_count:     40
    .vgpr_spill_count: 0
    .wavefront_size: 64
